# v34 + gate/up: lower wave group's alignment barrier moved ~100 instructions into its epilogue (starts epilogue during the other group's last MMA segment); epilogue-top vmcnt(0)->vmcnt(16)
# baseline (speedup 1.0000x reference)
.LBB0_252:
	s_nop 15
	s_nop 15
	v_ashrrev_i32_e32 v23, 31, v22
	s_ashr_i32 s67, s66, 31
	s_add_u32 s100, s50, s66
	s_addc_u32 s101, s51, s67
	s_add_u32 s100, s100, s52
	s_addc_u32 s101, s101, s53
	v_lshlrev_b64 v[250:251], 10, v[22:23]
	v_lshl_add_u64 v[250:251], v[250:251], 0, s[100:101]
	v_lshl_add_u64 v[250:251], v[250:251], 0, v[166:167]
	s_mov_b64 s[26:27], -1
	s_and_b64 vcc, exec, s[38:39]
	s_waitcnt vmcnt(16)
	s_waitcnt lgkmcnt(0)
	v_mov_b32_e32 v230, 0xc0c00000
	v_mov_b32_e32 v231, 0x41000000
	v_pk_add_f32 v[6:7], v[6:7], 1.0 op_sel_hi:[1,0]
	v_pk_add_f32 v[8:9], v[8:9], 1.0 op_sel_hi:[1,0]
	v_pk_add_f32 v[14:15], v[14:15], 1.0 op_sel_hi:[1,0]
	v_pk_add_f32 v[16:17], v[16:17], 1.0 op_sel_hi:[1,0]
	v_pk_fma_f32 v[26:27], v[154:155], s[24:25], v[2:3] op_sel_hi:[1,0,1]
	v_pk_fma_f32 v[18:19], v[160:161], s[24:25], v[12:13] op_sel_hi:[1,0,1]
	v_pk_fma_f32 v[20:21], v[158:159], s[24:25], v[10:11] op_sel_hi:[1,0,1]
	v_min_f32_e32 v18, 0x40e00000, v18
	v_min_f32_e32 v20, 0x40e00000, v20
	v_min_f32_e32 v21, 0x40e00000, v21
	v_pk_fma_f32 v[30:31], v[150:151], s[24:25], v[6:7] op_sel_hi:[1,0,1]
	v_min_f32_e32 v19, 0x40e00000, v19
	v_med3_f32 v30, v30, v230, v231
	v_med3_f32 v31, v31, v230, v231
	v_pk_fma_f32 v[32:33], v[148:149], s[24:25], v[16:17] op_sel_hi:[1,0,1]
	v_pk_mul_f32 v[148:149], v[20:21], s[28:29] op_sel_hi:[1,0]
	v_pk_mul_f32 v[20:21], v[20:21], v[30:31]
	v_pk_mul_f32 v[30:31], v[18:19], s[28:29] op_sel_hi:[1,0]
	v_pk_fma_f32 v[24:25], v[152:153], s[24:25], v[8:9] op_sel_hi:[1,0,1]
	v_exp_f32_e32 v30, v30
	v_exp_f32_e32 v31, v31
	v_med3_f32 v24, v24, v230, v231
	v_med3_f32 v25, v25, v230, v231
	v_pk_add_f32 v[30:31], v[30:31], 1.0 op_sel_hi:[1,0]
	v_pk_mul_f32 v[18:19], v[18:19], v[24:25]
	v_rcp_f32_e32 v30, v30
	v_rcp_f32_e32 v31, v31
	v_pk_fma_f32 v[146:147], v[146:147], s[24:25], v[14:15] op_sel_hi:[1,0,1]
	v_pk_fma_f32 v[28:29], v[156:157], s[24:25], v[4:5] op_sel_hi:[1,0,1]
	v_exp_f32_e32 v148, v148
	v_pk_mul_f32 v[24:25], v[18:19], v[30:31]
	v_min_f32_e32 v18, 0x40e00000, v26
	v_min_f32_e32 v19, 0x40e00000, v27
	v_pk_mul_f32 v[30:31], v[18:19], s[28:29] op_sel_hi:[1,0]
	v_med3_f32 v26, v146, v230, v231
	v_exp_f32_e32 v30, v30
	v_exp_f32_e32 v31, v31
	v_med3_f32 v27, v147, v230, v231
	v_exp_f32_e32 v149, v149
	v_pk_add_f32 v[30:31], v[30:31], 1.0 op_sel_hi:[1,0]
	v_pk_mul_f32 v[18:19], v[18:19], v[26:27]
	v_rcp_f32_e32 v30, v30
	v_rcp_f32_e32 v31, v31
	v_pk_add_f32 v[148:149], v[148:149], 1.0 op_sel_hi:[1,0]
	v_pk_fma_f32 v[134:135], v[134:135], s[24:25], v[6:7] op_sel_hi:[1,0,1]
	v_rcp_f32_e32 v148, v148
	v_pk_mul_f32 v[26:27], v[18:19], v[30:31]
	v_min_f32_e32 v18, 0x40e00000, v28
	v_min_f32_e32 v19, 0x40e00000, v29
	v_pk_mul_f32 v[30:31], v[18:19], s[28:29] op_sel_hi:[1,0]
	v_rcp_f32_e32 v149, v149
	v_exp_f32_e32 v30, v30
	v_exp_f32_e32 v31, v31
	v_med3_f32 v28, v32, v230, v231
	v_med3_f32 v29, v33, v230, v231
	v_pk_add_f32 v[30:31], v[30:31], 1.0 op_sel_hi:[1,0]
	v_pk_mul_f32 v[18:19], v[18:19], v[28:29]
	v_rcp_f32_e32 v30, v30
	v_rcp_f32_e32 v31, v31
	v_pk_mul_f32 v[20:21], v[20:21], v[148:149]
	v_pk_fma_f32 v[32:33], v[136:137], s[24:25], v[8:9] op_sel_hi:[1,0,1]
	v_pk_fma_f32 v[142:143], v[142:143], s[24:25], v[10:11] op_sel_hi:[1,0,1]
	v_pk_mul_f32 v[28:29], v[18:19], v[30:31]
	v_cvt_pk_fp8_f32 v19, v26, v27
	v_cvt_pk_fp8_f32 v18, v20, v21
	v_pk_fma_f32 v[30:31], v[144:145], s[24:25], v[12:13] op_sel_hi:[1,0,1]
	v_pk_fma_f32 v[20:21], v[140:141], s[24:25], v[4:5] op_sel_hi:[1,0,1]
	v_cvt_pk_fp8_f32 v19, v28, v29 op_sel:[0,0,1]
	v_pk_fma_f32 v[28:29], v[130:131], s[24:25], v[14:15] op_sel_hi:[1,0,1]
	v_cvt_pk_fp8_f32 v18, v24, v25 op_sel:[0,0,1]
	v_pk_fma_f32 v[26:27], v[138:139], s[24:25], v[2:3] op_sel_hi:[1,0,1]
	v_pk_fma_f32 v[24:25], v[132:133], s[24:25], v[16:17] op_sel_hi:[1,0,1]
	v_med3_f32 v132, v134, v230, v231
	v_med3_f32 v133, v135, v230, v231
	v_med3_f32 v32, v32, v230, v231
	v_med3_f32 v33, v33, v230, v231
	v_med3_f32 v28, v28, v230, v231
	v_med3_f32 v29, v29, v230, v231
	v_min_f32_e32 v130, 0x40e00000, v142
	v_min_f32_e32 v131, 0x40e00000, v143
	v_min_f32_e32 v30, 0x40e00000, v30
	v_min_f32_e32 v31, 0x40e00000, v31
	v_min_f32_e32 v26, 0x40e00000, v26
	s_cmp_lg_u64 s[58:59], 0
	s_cbranch_scc0 .Llate_gu
	s_barrier
.Llate_gu:
	v_min_f32_e32 v27, 0x40e00000, v27
	v_min_f32_e32 v20, 0x40e00000, v20
	v_min_f32_e32 v21, 0x40e00000, v21
	v_pk_mul_f32 v[134:135], v[130:131], s[28:29] op_sel_hi:[1,0]
	v_pk_mul_f32 v[130:131], v[130:131], v[132:133]
	v_pk_mul_f32 v[132:133], v[30:31], s[28:29] op_sel_hi:[1,0]
	v_pk_mul_f32 v[30:31], v[30:31], v[32:33]
	v_pk_mul_f32 v[32:33], v[26:27], s[28:29] op_sel_hi:[1,0]
	v_pk_mul_f32 v[26:27], v[26:27], v[28:29]
	v_pk_mul_f32 v[28:29], v[20:21], s[28:29] op_sel_hi:[1,0]
	v_exp_f32_e32 v134, v134
	v_exp_f32_e32 v135, v135
	v_exp_f32_e32 v32, v32
	v_exp_f32_e32 v33, v33
	v_exp_f32_e32 v28, v28
	v_exp_f32_e32 v29, v29
	v_pk_add_f32 v[134:135], v[134:135], 1.0 op_sel_hi:[1,0]
	v_exp_f32_e32 v132, v132
	v_exp_f32_e32 v133, v133
	v_pk_add_f32 v[32:33], v[32:33], 1.0 op_sel_hi:[1,0]
	v_pk_add_f32 v[28:29], v[28:29], 1.0 op_sel_hi:[1,0]
	v_rcp_f32_e32 v134, v134
	v_rcp_f32_e32 v135, v135
	v_rcp_f32_e32 v32, v32
	v_rcp_f32_e32 v33, v33
	v_rcp_f32_e32 v28, v28
	v_rcp_f32_e32 v29, v29
	v_med3_f32 v24, v24, v230, v231
	v_med3_f32 v25, v25, v230, v231
	v_pk_add_f32 v[132:133], v[132:133], 1.0 op_sel_hi:[1,0]
	v_pk_mul_f32 v[20:21], v[20:21], v[24:25]
	v_pk_mul_f32 v[130:131], v[130:131], v[134:135]
	v_rcp_f32_e32 v132, v132
	v_rcp_f32_e32 v133, v133
	v_pk_mul_f32 v[26:27], v[26:27], v[32:33]
	v_pk_mul_f32 v[24:25], v[20:21], v[28:29]
	v_cvt_pk_fp8_f32 v20, v130, v131
	v_cvt_pk_fp8_f32 v21, v26, v27
	v_pk_mul_f32 v[30:31], v[30:31], v[132:133]
	v_pk_fma_f32 v[32:33], v[116:117], s[24:25], v[16:17] op_sel_hi:[1,0,1]
	v_cvt_pk_fp8_f32 v20, v30, v31 op_sel:[0,0,1]
	v_cvt_pk_fp8_f32 v21, v24, v25 op_sel:[0,0,1]
	v_permlane16_swap_b32_e32 v18, v20
	v_permlane16_swap_b32_e32 v19, v21
	v_pk_fma_f32 v[30:31], v[118:119], s[24:25], v[6:7] op_sel_hi:[1,0,1]
	global_store_dwordx4 v[250:251], v[18:21], off
	v_med3_f32 v30, v30, v230, v231
	v_med3_f32 v31, v31, v230, v231
	v_pk_fma_f32 v[18:19], v[128:129], s[24:25], v[12:13] op_sel_hi:[1,0,1]
	v_pk_fma_f32 v[20:21], v[126:127], s[24:25], v[10:11] op_sel_hi:[1,0,1]
	v_min_f32_e32 v20, 0x40e00000, v20
	v_min_f32_e32 v21, 0x40e00000, v21
	v_min_f32_e32 v18, 0x40e00000, v18
	v_min_f32_e32 v19, 0x40e00000, v19
	v_pk_mul_f32 v[116:117], v[20:21], s[28:29] op_sel_hi:[1,0]
	v_pk_mul_f32 v[20:21], v[20:21], v[30:31]
	v_pk_mul_f32 v[30:31], v[18:19], s[28:29] op_sel_hi:[1,0]
	v_pk_fma_f32 v[28:29], v[120:121], s[24:25], v[8:9] op_sel_hi:[1,0,1]
	v_exp_f32_e32 v30, v30
	v_exp_f32_e32 v31, v31
	v_med3_f32 v28, v28, v230, v231
	v_med3_f32 v29, v29, v230, v231
	v_pk_add_f32 v[30:31], v[30:31], 1.0 op_sel_hi:[1,0]
	v_pk_fma_f32 v[26:27], v[122:123], s[24:25], v[2:3] op_sel_hi:[1,0,1]
	v_rcp_f32_e32 v30, v30
	v_rcp_f32_e32 v31, v31
	v_pk_mul_f32 v[18:19], v[18:19], v[28:29]
	v_pk_fma_f32 v[114:115], v[114:115], s[24:25], v[14:15] op_sel_hi:[1,0,1]
	v_pk_fma_f32 v[24:25], v[124:125], s[24:25], v[4:5] op_sel_hi:[1,0,1]
	v_pk_mul_f32 v[28:29], v[18:19], v[30:31]
	v_min_f32_e32 v18, 0x40e00000, v26
	v_min_f32_e32 v19, 0x40e00000, v27
	v_pk_mul_f32 v[30:31], v[18:19], s[28:29] op_sel_hi:[1,0]
	v_med3_f32 v26, v114, v230, v231
	v_exp_f32_e32 v30, v30
	v_exp_f32_e32 v31, v31
	v_med3_f32 v27, v115, v230, v231
	v_exp_f32_e32 v116, v116
	v_pk_add_f32 v[30:31], v[30:31], 1.0 op_sel_hi:[1,0]
	v_pk_mul_f32 v[18:19], v[18:19], v[26:27]
	v_rcp_f32_e32 v30, v30
	v_rcp_f32_e32 v31, v31
	v_exp_f32_e32 v117, v117
	v_pk_fma_f32 v[98:99], v[98:99], s[24:25], v[14:15] op_sel_hi:[1,0,1]
	v_pk_fma_f32 v[100:101], v[100:101], s[24:25], v[16:17] op_sel_hi:[1,0,1]
	v_pk_mul_f32 v[26:27], v[18:19], v[30:31]
	v_min_f32_e32 v18, 0x40e00000, v24
	v_min_f32_e32 v19, 0x40e00000, v25
	v_pk_mul_f32 v[30:31], v[18:19], s[28:29] op_sel_hi:[1,0]
	v_med3_f32 v24, v32, v230, v231
	v_exp_f32_e32 v30, v30
	v_exp_f32_e32 v31, v31
	v_med3_f32 v25, v33, v230, v231
	v_pk_add_f32 v[116:117], v[116:117], 1.0 op_sel_hi:[1,0]
	v_pk_add_f32 v[30:31], v[30:31], 1.0 op_sel_hi:[1,0]
	v_pk_mul_f32 v[18:19], v[18:19], v[24:25]
	v_rcp_f32_e32 v30, v30
	v_rcp_f32_e32 v31, v31
	v_rcp_f32_e32 v116, v116
	v_rcp_f32_e32 v117, v117
	v_pk_fma_f32 v[32:33], v[102:103], s[24:25], v[6:7] op_sel_hi:[1,0,1]
	v_pk_mul_f32 v[24:25], v[18:19], v[30:31]
	v_cvt_pk_fp8_f32 v19, v26, v27
	v_pk_mul_f32 v[20:21], v[20:21], v[116:117]
	v_cvt_pk_fp8_f32 v18, v20, v21
	v_cvt_pk_fp8_f32 v19, v24, v25 op_sel:[0,0,1]
	v_pk_fma_f32 v[20:21], v[112:113], s[24:25], v[12:13] op_sel_hi:[1,0,1]
	v_pk_fma_f32 v[24:25], v[110:111], s[24:25], v[10:11] op_sel_hi:[1,0,1]
	v_med3_f32 v32, v32, v230, v231
	v_med3_f32 v33, v33, v230, v231
	v_min_f32_e32 v24, 0x40e00000, v24
	v_min_f32_e32 v25, 0x40e00000, v25
	v_min_f32_e32 v20, 0x40e00000, v20
	v_min_f32_e32 v21, 0x40e00000, v21
	v_pk_mul_f32 v[102:103], v[24:25], s[28:29] op_sel_hi:[1,0]
	v_pk_mul_f32 v[24:25], v[24:25], v[32:33]
	v_pk_mul_f32 v[32:33], v[20:21], s[28:29] op_sel_hi:[1,0]
	v_pk_fma_f32 v[30:31], v[104:105], s[24:25], v[8:9] op_sel_hi:[1,0,1]
	v_exp_f32_e32 v32, v32
	v_exp_f32_e32 v33, v33
	v_med3_f32 v30, v30, v230, v231
	v_med3_f32 v31, v31, v230, v231
	v_pk_add_f32 v[32:33], v[32:33], 1.0 op_sel_hi:[1,0]
	v_cvt_pk_fp8_f32 v18, v28, v29 op_sel:[0,0,1]
	v_rcp_f32_e32 v32, v32
	v_rcp_f32_e32 v33, v33
	v_pk_fma_f32 v[28:29], v[106:107], s[24:25], v[2:3] op_sel_hi:[1,0,1]
	v_pk_mul_f32 v[20:21], v[20:21], v[30:31]
	v_pk_fma_f32 v[26:27], v[108:109], s[24:25], v[4:5] op_sel_hi:[1,0,1]
	v_pk_mul_f32 v[30:31], v[20:21], v[32:33]
	v_min_f32_e32 v20, 0x40e00000, v28
	v_min_f32_e32 v21, 0x40e00000, v29
	v_pk_mul_f32 v[32:33], v[20:21], s[28:29] op_sel_hi:[1,0]
	v_med3_f32 v28, v98, v230, v231
	v_exp_f32_e32 v32, v32
	v_exp_f32_e32 v33, v33
	v_med3_f32 v29, v99, v230, v231
	v_exp_f32_e32 v102, v102
	v_pk_add_f32 v[32:33], v[32:33], 1.0 op_sel_hi:[1,0]
	v_pk_mul_f32 v[20:21], v[20:21], v[28:29]
	v_rcp_f32_e32 v32, v32
	v_rcp_f32_e32 v33, v33
	v_exp_f32_e32 v103, v103
	v_pk_fma_f32 v[82:83], v[82:83], s[24:25], v[14:15] op_sel_hi:[1,0,1]
	v_pk_fma_f32 v[84:85], v[84:85], s[24:25], v[16:17] op_sel_hi:[1,0,1]
	v_pk_mul_f32 v[28:29], v[20:21], v[32:33]
	v_min_f32_e32 v20, 0x40e00000, v26
	v_min_f32_e32 v21, 0x40e00000, v27
	v_pk_mul_f32 v[32:33], v[20:21], s[28:29] op_sel_hi:[1,0]
	v_pk_add_f32 v[102:103], v[102:103], 1.0 op_sel_hi:[1,0]
	v_exp_f32_e32 v32, v32
	v_exp_f32_e32 v33, v33
	v_rcp_f32_e32 v102, v102
	v_rcp_f32_e32 v103, v103
	v_med3_f32 v26, v100, v230, v231
	v_pk_add_f32 v[32:33], v[32:33], 1.0 op_sel_hi:[1,0]
	v_med3_f32 v27, v101, v230, v231
	v_rcp_f32_e32 v32, v32
	v_rcp_f32_e32 v33, v33
	v_pk_mul_f32 v[24:25], v[24:25], v[102:103]
	v_pk_mul_f32 v[20:21], v[20:21], v[26:27]
	s_nop 0
	v_pk_mul_f32 v[26:27], v[20:21], v[32:33]
	v_cvt_pk_fp8_f32 v20, v24, v25
	v_cvt_pk_fp8_f32 v21, v28, v29
	v_cvt_pk_fp8_f32 v20, v30, v31 op_sel:[0,0,1]
	v_cvt_pk_fp8_f32 v21, v26, v27 op_sel:[0,0,1]
	v_permlane16_swap_b32_e32 v18, v20
	v_permlane16_swap_b32_e32 v19, v21
	s_mov_b64 s[100:101], 0x8000
	v_lshl_add_u64 v[24:25], v[250:251], 0, s[100:101]
	v_pk_fma_f32 v[32:33], v[86:87], s[24:25], v[6:7] op_sel_hi:[1,0,1]
	global_store_dwordx4 v[24:25], v[18:21], off
	v_med3_f32 v32, v32, v230, v231
	v_med3_f32 v33, v33, v230, v231
	v_pk_fma_f32 v[18:19], v[96:97], s[24:25], v[12:13] op_sel_hi:[1,0,1]
	v_pk_fma_f32 v[20:21], v[94:95], s[24:25], v[10:11] op_sel_hi:[1,0,1]
	v_min_f32_e32 v20, 0x40e00000, v20
	v_min_f32_e32 v21, 0x40e00000, v21
	v_min_f32_e32 v18, 0x40e00000, v18
	v_min_f32_e32 v19, 0x40e00000, v19
	v_pk_mul_f32 v[86:87], v[20:21], s[28:29] op_sel_hi:[1,0]
	v_pk_mul_f32 v[20:21], v[20:21], v[32:33]
	v_pk_mul_f32 v[32:33], v[18:19], s[28:29] op_sel_hi:[1,0]
	v_pk_fma_f32 v[30:31], v[88:89], s[24:25], v[8:9] op_sel_hi:[1,0,1]
	v_exp_f32_e32 v32, v32
	v_exp_f32_e32 v33, v33
	v_med3_f32 v30, v30, v230, v231
	v_med3_f32 v31, v31, v230, v231
	v_pk_add_f32 v[32:33], v[32:33], 1.0 op_sel_hi:[1,0]
	v_pk_fma_f32 v[28:29], v[90:91], s[24:25], v[2:3] op_sel_hi:[1,0,1]
	v_rcp_f32_e32 v32, v32
	v_rcp_f32_e32 v33, v33
	v_pk_mul_f32 v[18:19], v[18:19], v[30:31]
	v_pk_fma_f32 v[26:27], v[92:93], s[24:25], v[4:5] op_sel_hi:[1,0,1]
	v_exp_f32_e32 v86, v86
	v_pk_mul_f32 v[30:31], v[18:19], v[32:33]
	v_min_f32_e32 v18, 0x40e00000, v28
	v_min_f32_e32 v19, 0x40e00000, v29
	v_pk_mul_f32 v[32:33], v[18:19], s[28:29] op_sel_hi:[1,0]
	v_med3_f32 v28, v82, v230, v231
	v_exp_f32_e32 v32, v32
	v_exp_f32_e32 v33, v33
	v_med3_f32 v29, v83, v230, v231
	v_exp_f32_e32 v87, v87
	v_pk_add_f32 v[32:33], v[32:33], 1.0 op_sel_hi:[1,0]
	v_pk_mul_f32 v[18:19], v[18:19], v[28:29]
	v_rcp_f32_e32 v32, v32
	v_rcp_f32_e32 v33, v33
	v_pk_add_f32 v[86:87], v[86:87], 1.0 op_sel_hi:[1,0]
	v_rcp_f32_e32 v86, v86
	v_pk_mul_f32 v[28:29], v[18:19], v[32:33]
	v_min_f32_e32 v18, 0x40e00000, v26
	v_min_f32_e32 v19, 0x40e00000, v27
	v_pk_mul_f32 v[32:33], v[18:19], s[28:29] op_sel_hi:[1,0]
	v_rcp_f32_e32 v87, v87
	v_exp_f32_e32 v32, v32
	v_exp_f32_e32 v33, v33
	v_med3_f32 v26, v84, v230, v231
	v_med3_f32 v27, v85, v230, v231
	v_pk_add_f32 v[32:33], v[32:33], 1.0 op_sel_hi:[1,0]
	v_pk_mul_f32 v[18:19], v[18:19], v[26:27]
	v_rcp_f32_e32 v32, v32
	v_rcp_f32_e32 v33, v33
	v_pk_mul_f32 v[20:21], v[20:21], v[86:87]
	v_pk_mul_f32 v[26:27], v[18:19], v[32:33]
	v_cvt_pk_fp8_f32 v18, v20, v21
	v_cvt_pk_fp8_f32 v19, v28, v29
	v_pk_fma_f32 v[20:21], v[72:73], s[24:25], v[12:13] op_sel_hi:[1,0,1]
	v_cvt_pk_fp8_f32 v18, v30, v31 op_sel:[0,0,1]
	v_pk_fma_f32 v[30:31], v[66:67], s[24:25], v[2:3] op_sel_hi:[1,0,1]
	v_pk_fma_f32 v[66:67], v[78:79], s[24:25], v[6:7] op_sel_hi:[1,0,1]
	v_cvt_pk_fp8_f32 v19, v26, v27 op_sel:[0,0,1]
	v_pk_fma_f32 v[26:27], v[70:71], s[24:25], v[10:11] op_sel_hi:[1,0,1]
	v_med3_f32 v66, v66, v230, v231
	v_med3_f32 v67, v67, v230, v231
	v_min_f32_e32 v26, 0x40e00000, v26
	v_min_f32_e32 v27, 0x40e00000, v27
	v_min_f32_e32 v20, 0x40e00000, v20
	v_min_f32_e32 v21, 0x40e00000, v21
	v_pk_mul_f32 v[72:73], v[26:27], s[28:29] op_sel_hi:[1,0]
	v_pk_mul_f32 v[26:27], v[26:27], v[66:67]
	v_pk_mul_f32 v[66:67], v[20:21], s[28:29] op_sel_hi:[1,0]
	v_pk_fma_f32 v[32:33], v[80:81], s[24:25], v[8:9] op_sel_hi:[1,0,1]
	v_exp_f32_e32 v66, v66
	v_exp_f32_e32 v67, v67
	v_med3_f32 v32, v32, v230, v231
	v_med3_f32 v33, v33, v230, v231
	v_pk_add_f32 v[66:67], v[66:67], 1.0 op_sel_hi:[1,0]
	v_pk_mul_f32 v[20:21], v[20:21], v[32:33]
	v_rcp_f32_e32 v66, v66
	v_rcp_f32_e32 v67, v67
	v_pk_fma_f32 v[70:71], v[74:75], s[24:25], v[14:15] op_sel_hi:[1,0,1]
	v_pk_fma_f32 v[28:29], v[68:69], s[24:25], v[4:5] op_sel_hi:[1,0,1]
	v_exp_f32_e32 v72, v72
	v_pk_mul_f32 v[32:33], v[20:21], v[66:67]
	v_min_f32_e32 v20, 0x40e00000, v30
	v_min_f32_e32 v21, 0x40e00000, v31
	v_pk_mul_f32 v[66:67], v[20:21], s[28:29] op_sel_hi:[1,0]
	v_med3_f32 v30, v70, v230, v231
	v_exp_f32_e32 v66, v66
	v_exp_f32_e32 v67, v67
	v_med3_f32 v31, v71, v230, v231
	v_exp_f32_e32 v73, v73
	v_pk_add_f32 v[66:67], v[66:67], 1.0 op_sel_hi:[1,0]
	v_pk_mul_f32 v[20:21], v[20:21], v[30:31]
	v_rcp_f32_e32 v66, v66
	v_rcp_f32_e32 v67, v67
	v_pk_add_f32 v[72:73], v[72:73], 1.0 op_sel_hi:[1,0]
	v_pk_fma_f32 v[68:69], v[76:77], s[24:25], v[16:17] op_sel_hi:[1,0,1]
	v_rcp_f32_e32 v72, v72
	v_pk_mul_f32 v[30:31], v[20:21], v[66:67]
	v_min_f32_e32 v20, 0x40e00000, v28
	v_min_f32_e32 v21, 0x40e00000, v29
	v_pk_mul_f32 v[66:67], v[20:21], s[28:29] op_sel_hi:[1,0]
	v_rcp_f32_e32 v73, v73
	v_exp_f32_e32 v66, v66
	v_exp_f32_e32 v67, v67
	v_med3_f32 v28, v68, v230, v231
	v_med3_f32 v29, v69, v230, v231
	v_pk_add_f32 v[66:67], v[66:67], 1.0 op_sel_hi:[1,0]
	v_pk_mul_f32 v[20:21], v[20:21], v[28:29]
	v_rcp_f32_e32 v66, v66
	v_rcp_f32_e32 v67, v67
	v_pk_mul_f32 v[26:27], v[26:27], v[72:73]
	v_pk_mul_f32 v[28:29], v[20:21], v[66:67]
	v_cvt_pk_fp8_f32 v20, v26, v27
	v_cvt_pk_fp8_f32 v21, v30, v31
	s_mov_b64 s[100:101], 0x20000
	v_lshl_add_u64 v[24:25], v[250:251], 0, s[100:101]
	v_cvt_pk_fp8_f32 v20, v32, v33 op_sel:[0,0,1]
	v_cvt_pk_fp8_f32 v21, v28, v29 op_sel:[0,0,1]
	v_pk_fma_f32 v[30:31], v[62:63], s[24:25], v[6:7] op_sel_hi:[1,0,1]
	v_pk_fma_f32 v[28:29], v[64:65], s[24:25], v[8:9] op_sel_hi:[1,0,1]
	v_permlane16_swap_b32_e32 v18, v20
	v_permlane16_swap_b32_e32 v19, v21
	global_store_dwordx4 v[24:25], v[18:21], off
	v_med3_f32 v30, v30, v230, v231
	v_med3_f32 v31, v31, v230, v231
	v_pk_fma_f32 v[18:19], v[56:57], s[24:25], v[12:13] op_sel_hi:[1,0,1]
	v_pk_fma_f32 v[20:21], v[54:55], s[24:25], v[10:11] op_sel_hi:[1,0,1]
	v_min_f32_e32 v20, 0x40e00000, v20
	v_min_f32_e32 v21, 0x40e00000, v21
	v_min_f32_e32 v18, 0x40e00000, v18
	v_min_f32_e32 v19, 0x40e00000, v19
	v_pk_fma_f32 v[24:25], v[52:53], s[24:25], v[4:5] op_sel_hi:[1,0,1]
	v_pk_mul_f32 v[52:53], v[20:21], s[28:29] op_sel_hi:[1,0]
	v_pk_mul_f32 v[20:21], v[20:21], v[30:31]
	v_pk_mul_f32 v[30:31], v[18:19], s[28:29] op_sel_hi:[1,0]
	v_med3_f32 v28, v28, v230, v231
	v_exp_f32_e32 v30, v30
	v_exp_f32_e32 v31, v31
	v_med3_f32 v29, v29, v230, v231
	v_pk_fma_f32 v[26:27], v[50:51], s[24:25], v[2:3] op_sel_hi:[1,0,1]
	v_pk_add_f32 v[30:31], v[30:31], 1.0 op_sel_hi:[1,0]
	v_pk_mul_f32 v[18:19], v[18:19], v[28:29]
	v_rcp_f32_e32 v30, v30
	v_rcp_f32_e32 v31, v31
	v_pk_fma_f32 v[50:51], v[58:59], s[24:25], v[14:15] op_sel_hi:[1,0,1]
	v_exp_f32_e32 v52, v52
	v_exp_f32_e32 v53, v53
	v_pk_mul_f32 v[28:29], v[18:19], v[30:31]
	v_min_f32_e32 v18, 0x40e00000, v26
	v_min_f32_e32 v19, 0x40e00000, v27
	v_pk_mul_f32 v[30:31], v[18:19], s[28:29] op_sel_hi:[1,0]
	v_med3_f32 v26, v50, v230, v231
	v_exp_f32_e32 v30, v30
	v_exp_f32_e32 v31, v31
	v_med3_f32 v27, v51, v230, v231
	v_pk_add_f32 v[52:53], v[52:53], 1.0 op_sel_hi:[1,0]
	v_pk_add_f32 v[30:31], v[30:31], 1.0 op_sel_hi:[1,0]
	v_pk_mul_f32 v[18:19], v[18:19], v[26:27]
	v_rcp_f32_e32 v30, v30
	v_rcp_f32_e32 v31, v31
	v_pk_fma_f32 v[32:33], v[60:61], s[24:25], v[16:17] op_sel_hi:[1,0,1]
	v_rcp_f32_e32 v52, v52
	v_rcp_f32_e32 v53, v53
	v_pk_mul_f32 v[26:27], v[18:19], v[30:31]
	v_min_f32_e32 v18, 0x40e00000, v24
	v_min_f32_e32 v19, 0x40e00000, v25
	v_pk_mul_f32 v[30:31], v[18:19], s[28:29] op_sel_hi:[1,0]
	v_med3_f32 v24, v32, v230, v231
	v_exp_f32_e32 v30, v30
	v_exp_f32_e32 v31, v31
	v_med3_f32 v25, v33, v230, v231
	v_pk_fma_f32 v[6:7], v[46:47], s[24:25], v[6:7] op_sel_hi:[1,0,1]
	v_pk_add_f32 v[30:31], v[30:31], 1.0 op_sel_hi:[1,0]
	v_pk_mul_f32 v[18:19], v[18:19], v[24:25]
	v_rcp_f32_e32 v30, v30
	v_rcp_f32_e32 v31, v31
	v_pk_fma_f32 v[10:11], v[38:39], s[24:25], v[10:11] op_sel_hi:[1,0,1]
	v_med3_f32 v6, v6, v230, v231
	v_med3_f32 v7, v7, v230, v231
	v_pk_mul_f32 v[20:21], v[20:21], v[52:53]
	v_pk_mul_f32 v[24:25], v[18:19], v[30:31]
	v_pk_fma_f32 v[12:13], v[40:41], s[24:25], v[12:13] op_sel_hi:[1,0,1]
	v_min_f32_e32 v10, 0x40e00000, v10
	v_min_f32_e32 v11, 0x40e00000, v11
	v_cvt_pk_fp8_f32 v18, v20, v21
	v_pk_mul_f32 v[20:21], v[10:11], s[28:29] op_sel_hi:[1,0]
	v_pk_mul_f32 v[6:7], v[10:11], v[6:7]
	v_min_f32_e32 v10, 0x40e00000, v12
	v_min_f32_e32 v11, 0x40e00000, v13
	v_pk_mul_f32 v[12:13], v[10:11], s[28:29] op_sel_hi:[1,0]
	v_pk_fma_f32 v[8:9], v[48:49], s[24:25], v[8:9] op_sel_hi:[1,0,1]
	v_exp_f32_e32 v12, v12
	v_exp_f32_e32 v13, v13
	v_med3_f32 v8, v8, v230, v231
	v_med3_f32 v9, v9, v230, v231
	v_pk_fma_f32 v[2:3], v[34:35], s[24:25], v[2:3] op_sel_hi:[1,0,1]
	v_pk_add_f32 v[12:13], v[12:13], 1.0 op_sel_hi:[1,0]
	v_rcp_f32_e32 v12, v12
	v_rcp_f32_e32 v13, v13
	v_pk_mul_f32 v[8:9], v[10:11], v[8:9]
	v_min_f32_e32 v2, 0x40e00000, v2
	v_min_f32_e32 v3, 0x40e00000, v3
	v_pk_mul_f32 v[8:9], v[8:9], v[12:13]
	v_pk_mul_f32 v[12:13], v[2:3], s[28:29] op_sel_hi:[1,0]
	v_pk_fma_f32 v[14:15], v[42:43], s[24:25], v[14:15] op_sel_hi:[1,0,1]
	v_exp_f32_e32 v12, v12
	v_exp_f32_e32 v13, v13
	v_exp_f32_e32 v20, v20
	v_exp_f32_e32 v21, v21
	v_med3_f32 v10, v14, v230, v231
	v_pk_add_f32 v[12:13], v[12:13], 1.0 op_sel_hi:[1,0]
	v_med3_f32 v11, v15, v230, v231
	v_rcp_f32_e32 v12, v12
	v_rcp_f32_e32 v13, v13
	v_pk_fma_f32 v[4:5], v[36:37], s[24:25], v[4:5] op_sel_hi:[1,0,1]
	v_min_f32_e32 v4, 0x40e00000, v4
	v_pk_mul_f32 v[2:3], v[2:3], v[10:11]
	v_min_f32_e32 v5, 0x40e00000, v5
	v_pk_mul_f32 v[2:3], v[2:3], v[12:13]
	v_pk_mul_f32 v[12:13], v[4:5], s[28:29] op_sel_hi:[1,0]
	v_pk_add_f32 v[20:21], v[20:21], 1.0 op_sel_hi:[1,0]
	v_exp_f32_e32 v12, v12
	v_exp_f32_e32 v13, v13
	v_rcp_f32_e32 v20, v20
	v_rcp_f32_e32 v21, v21
	v_pk_add_f32 v[12:13], v[12:13], 1.0 op_sel_hi:[1,0]
	v_pk_fma_f32 v[16:17], v[44:45], s[24:25], v[16:17] op_sel_hi:[1,0,1]
	v_pk_mul_f32 v[6:7], v[6:7], v[20:21]
	v_rcp_f32_e32 v12, v12
	v_rcp_f32_e32 v13, v13
	v_cvt_pk_fp8_f32 v19, v26, v27
	v_med3_f32 v10, v16, v230, v231
	v_med3_f32 v11, v17, v230, v231
	v_cvt_pk_fp8_f32 v20, v6, v7
	v_cvt_pk_fp8_f32 v21, v2, v3
	v_pk_mul_f32 v[4:5], v[4:5], v[10:11]
	v_pk_mul_f32 v[4:5], v[4:5], v[12:13]
	v_cvt_pk_fp8_f32 v18, v28, v29 op_sel:[0,0,1]
	v_cvt_pk_fp8_f32 v19, v24, v25 op_sel:[0,0,1]
	v_cvt_pk_fp8_f32 v20, v8, v9 op_sel:[0,0,1]
	v_cvt_pk_fp8_f32 v21, v4, v5 op_sel:[0,0,1]
	v_permlane16_swap_b32_e32 v18, v20
	v_permlane16_swap_b32_e32 v19, v21
	s_mov_b64 s[100:101], 0x28000
	v_lshl_add_u64 v[2:3], v[250:251], 0, s[100:101]
	global_store_dwordx4 v[2:3], v[18:21], off
	s_cbranch_vccnz .LBB0_237
	s_andn2_b64 vcc, exec, s[42:43]
	s_cbranch_vccnz .LBB0_236
	s_barrier
	s_branch .LBB0_236
